# attention PV block: first 8 V transpose-reads issued early (end of the QK block) into free registers v186-v201, second 8 issued at PV start; PV MFMAs no longer start on an exposed LDS latency
# speedup vs baseline: 1.0021x; 1.0021x over previous
.LBB0_582:
	ds_read_b128 v[34:37], v145 offset:32768
	ds_read_b128 v[38:41], v145 offset:40960
	ds_read_b128 v[162:165], v148 offset:32768
	ds_read_b128 v[172:175], v148 offset:40960
	v_exp_f32_e32 v161, v114
	v_add_f32_e32 v114, 0, v128
	s_waitcnt lgkmcnt(3)
	v_mfma_f32_32x32x16_bf16 v[50:65], v[34:37], v[86:89], 0
	v_add_f32_e32 v114, v157, v114
	v_add_f32_e32 v114, v129, v114
	v_add_f32_e32 v114, v158, v114
	v_add_f32_e32 v114, v155, v114
	v_add_f32_e32 v114, v159, v114
	v_add_f32_e32 v114, v156, v114
	v_add_f32_e32 v114, v160, v114
	s_waitcnt lgkmcnt(2)
	v_mfma_f32_32x32x16_bf16 v[34:49], v[38:41], v[86:89], 0
	v_add_f32_e32 v114, v120, v114
	v_add_f32_e32 v114, v124, v114
	v_add_f32_e32 v114, v121, v114
	v_add_f32_e32 v114, v125, v114
	v_exp_f32_e32 v119, v116
	v_add_f32_e32 v114, v122, v114
	v_exp_f32_e32 v154, v117
	s_waitcnt lgkmcnt(1)
	v_mfma_f32_32x32x16_bf16 v[50:65], v[162:165], v[74:77], v[50:65]
	v_add_f32_e32 v114, v126, v114
	v_add_f32_e32 v114, v123, v114
	v_add_f32_e32 v114, v127, v114
	v_exp_f32_e32 v112, v112
	v_add_f32_e32 v114, v119, v114
	v_exp_f32_e32 v113, v113
	v_add_f32_e32 v114, v154, v114
	s_waitcnt lgkmcnt(0)
	v_mfma_f32_32x32x16_bf16 v[34:49], v[172:175], v[74:77], v[34:49]
	ds_read_b128 v[162:165], v147 offset:32768
	ds_read_b128 v[172:175], v147 offset:40960
	v_exp_f32_e32 v106, v106
	v_add_f32_e32 v114, v161, v114
	v_exp_f32_e32 v107, v107
	v_exp_f32_e32 v104, v104
	v_exp_f32_e32 v105, v105
	v_exp_f32_e32 v110, v110
	s_waitcnt lgkmcnt(1)
	v_mfma_f32_32x32x16_bf16 v[50:65], v[162:165], v[70:73], v[50:65]
	v_exp_f32_e32 v111, v111
	v_exp_f32_e32 v108, v108
	v_exp_f32_e32 v109, v109
	v_exp_f32_e32 v102, v102
	v_exp_f32_e32 v103, v103
	s_waitcnt lgkmcnt(0)
	v_mfma_f32_32x32x16_bf16 v[34:49], v[172:175], v[70:73], v[34:49]
	ds_read_b128 v[162:165], v146 offset:32768
	ds_read_b128 v[172:175], v146 offset:40960
	s_waitcnt lgkmcnt(1)
	v_mfma_f32_32x32x16_bf16 v[50:65], v[162:165], v[82:85], v[50:65]
	s_waitcnt lgkmcnt(0)
	v_mfma_f32_32x32x16_bf16 v[34:49], v[172:175], v[82:85], v[34:49]
	ds_read_b128 v[162:165], v150 offset:32768
	ds_read_b128 v[172:175], v150 offset:40960
	s_waitcnt lgkmcnt(1)
	v_mfma_f32_32x32x16_bf16 v[50:65], v[162:165], v[78:81], v[50:65]
	s_waitcnt lgkmcnt(0)
	v_mfma_f32_32x32x16_bf16 v[34:49], v[172:175], v[78:81], v[34:49]
	ds_read_b128 v[162:165], v149 offset:32768
	ds_read_b128 v[172:175], v149 offset:40960
	s_waitcnt lgkmcnt(1)
	v_mfma_f32_32x32x16_bf16 v[50:65], v[162:165], v[66:69], v[50:65]
	v_exp_f32_e32 v162, v115
	s_nop 0
	v_add_f32_e32 v114, v162, v114
	v_add_f32_e32 v114, v112, v114
	v_add_f32_e32 v114, v113, v114
	v_add_f32_e32 v114, v106, v114
	v_add_f32_e32 v114, v107, v114
	v_add_f32_e32 v114, v104, v114
	v_add_f32_e32 v114, v105, v114
	s_waitcnt lgkmcnt(0)
	v_mfma_f32_32x32x16_bf16 v[34:49], v[172:175], v[66:69], v[34:49]
	ds_read_b64_tr_b16 v[186:187], v141 offset:0
	ds_read_b64_tr_b16 v[188:189], v141 offset:0x400
	ds_read_b64_tr_b16 v[190:191], v141 offset:0x800
	ds_read_b64_tr_b16 v[192:193], v141 offset:0xc00
	ds_read_b64_tr_b16 v[194:195], v141 offset:0x1000
	ds_read_b64_tr_b16 v[196:197], v141 offset:0x1400
	ds_read_b64_tr_b16 v[198:199], v141 offset:0x1800
	ds_read_b64_tr_b16 v[200:201], v141 offset:0x1c00
	v_add_f32_e32 v114, v110, v114
	v_add_f32_e32 v114, v111, v114
	v_add_f32_e32 v114, v108, v114
	v_add_f32_e32 v114, v109, v114
	v_add_f32_e32 v114, v102, v114
	v_add_f32_e32 v152, v103, v114
	v_mov_b32_e32 v153, v152
	v_cvt_pk_bf16_f32 v114, v128, v157
	v_cvt_pk_bf16_f32 v115, v129, v158
	v_cvt_pk_bf16_f32 v116, v155, v159
	v_cvt_pk_bf16_f32 v117, v156, v160
	v_cvt_pk_bf16_f32 v120, v120, v124
	v_cvt_pk_bf16_f32 v121, v121, v125
	v_cvt_pk_bf16_f32 v122, v122, v126
	v_cvt_pk_bf16_f32 v123, v123, v127
	v_cvt_pk_bf16_f32 v124, v119, v154
	v_cvt_pk_bf16_f32 v125, v161, v162
	v_cvt_pk_bf16_f32 v126, v112, v113
	v_cvt_pk_bf16_f32 v127, v106, v107
	v_cvt_pk_bf16_f32 v154, v104, v105
	v_cvt_pk_bf16_f32 v155, v110, v111
	v_cvt_pk_bf16_f32 v156, v108, v109
	s_nop 1
	v_permlane32_swap_b32_e32 v152, v153
	v_permlane32_swap_b32_e32 v114, v116
	v_cvt_pk_bf16_f32 v157, v102, v103
	v_permlane32_swap_b32_e32 v154, v156
	v_permlane32_swap_b32_e32 v115, v117
	v_permlane32_swap_b32_e32 v120, v122
	v_permlane32_swap_b32_e32 v121, v123
	v_permlane32_swap_b32_e32 v124, v126
	v_permlane32_swap_b32_e32 v125, v127
	v_permlane32_swap_b32_e32 v155, v157
	s_movk_i32 s0, 0xe000
	v_add_co_u32_e32 v102, vcc, s0, v134
	s_movk_i32 s0, 0xa000
	s_nop 0
	v_addc_co_u32_e32 v103, vcc, -1, v135, vcc
	v_add_co_u32_e32 v106, vcc, s0, v132
	s_movk_i32 s0, 0xc000
	s_nop 0
	v_addc_co_u32_e32 v107, vcc, -1, v133, vcc
	v_add_co_u32_e32 v110, vcc, s0, v132
	global_load_dwordx4 v[102:105], v[102:103], off
	s_nop 0
	v_addc_co_u32_e32 v111, vcc, -1, v133, vcc
	global_load_dwordx4 v[106:109], v[106:107], off
	s_nop 0
	global_load_dwordx4 v[110:113], v[110:111], off
	ds_read_b64_tr_b16 v[158:159], v141 offset:0x200
	ds_read_b64_tr_b16 v[160:161], v141 offset:0x600
	ds_read_b64_tr_b16 v[162:163], v141 offset:0xa00
	ds_read_b64_tr_b16 v[164:165], v141 offset:0xe00
	ds_read_b64_tr_b16 v[172:173], v141 offset:0x1200
	ds_read_b64_tr_b16 v[174:175], v141 offset:0x1600
	ds_read_b64_tr_b16 v[176:177], v141 offset:0x1a00
	ds_read_b64_tr_b16 v[178:179], v141 offset:0x1e00
	s_waitcnt lgkmcnt(8)
	s_nop 0
	v_mfma_f32_32x32x16_bf16 v[2:17], v[114:117], v[186:189], v[2:17]
	v_mfma_f32_32x32x16_bf16 v[2:17], v[120:123], v[190:193], v[2:17]
	v_mfma_f32_32x32x16_bf16 v[2:17], v[124:127], v[194:197], v[2:17]
	v_mfma_f32_32x32x16_bf16 v[2:17], v[154:157], v[198:201], v[2:17]
	s_waitcnt lgkmcnt(0)
	v_mfma_f32_32x32x16_bf16 v[18:33], v[114:117], v[158:161], v[18:33]
	v_max_f32_e32 v114, v51, v51
	v_max_f32_e32 v115, v50, v50
	v_max_f32_e32 v114, v115, v114
	v_max3_f32 v114, v114, v52, v53
	v_max3_f32 v114, v114, v54, v55
	v_max3_f32 v114, v114, v56, v57
	v_max3_f32 v114, v114, v58, v59
	v_max3_f32 v114, v114, v60, v61
	v_max3_f32 v114, v114, v62, v63
	v_mfma_f32_32x32x16_bf16 v[18:33], v[120:123], v[162:165], v[18:33]
	v_max3_f32 v114, v114, v64, v65
	v_max3_f32 v114, v114, v34, v35
	v_max3_f32 v114, v114, v36, v37
	v_max3_f32 v114, v114, v38, v39
	v_max3_f32 v114, v114, v40, v41
	v_max3_f32 v114, v114, v42, v43
	v_max3_f32 v114, v114, v44, v45
	v_max3_f32 v114, v114, v46, v47
	v_mfma_f32_32x32x16_bf16 v[18:33], v[124:127], v[172:175], v[18:33]
	v_max3_f32 v114, v114, v48, v49
	v_mov_b32_e32 v115, v114
	s_nop 1
	v_permlane32_swap_b32_e32 v114, v115
	v_max_f32_e32 v115, v115, v115
	v_max_f32_e32 v114, v114, v114
	v_max_f32_e32 v114, v114, v115
	v_sub_f32_e32 v115, v114, v118
	v_cmp_ge_f32_e32 vcc, s93, v115
	v_max_f32_e32 v115, v118, v118
	v_max_f32_e32 v114, v115, v114
	v_mfma_f32_32x32x16_bf16 v[18:33], v[154:157], v[176:179], v[18:33]
	v_sub_f32_e32 v115, v118, v114
	v_mul_f32_e32 v115, 0x3fb8aa3b, v115
	v_exp_f32_e32 v115, v115
	s_cmp_eq_u64 vcc, exec
	s_cselect_b64 s[6:7], -1, 0
	s_barrier
	s_waitcnt vmcnt(3)
	v_cndmask_b32_e64 v154, v115, 1.0, s[6:7]
	v_cmp_gt_f32_e32 vcc, 1.0, v154
	s_waitcnt vmcnt(3)
	ds_write_b128 v144, v[90:93]
	ds_write_b128 v142, v[98:101] offset:16384
	ds_write_b128 v143, v[94:97] offset:16384
	s_cbranch_vccz .LBB0_586
	s_and_saveexec_b64 s[0:1], s[4:5]
	ds_write_b32 v138, v154 offset:49280
	s_or_b64 exec, exec, s[0:1]
	s_waitcnt lgkmcnt(0)
	v_add_u32_e32 v115, v131, v226
	ds_read_b128 v[120:123], v115 offset:49376
	ds_read_b128 v[124:127], v115 offset:49344
	ds_read_b128 v[156:159], v115 offset:49312
	ds_read_b128 v[160:163], v115 offset:49280
	s_waitcnt lgkmcnt(3)
	v_pk_mul_f32 v[14:15], v[14:15], v[120:121]
	s_waitcnt lgkmcnt(2)
	v_pk_mul_f32 v[10:11], v[10:11], v[124:125]
	s_waitcnt lgkmcnt(1)
	v_pk_mul_f32 v[6:7], v[6:7], v[156:157]
	v_pk_mul_f32 v[16:17], v[16:17], v[122:123]
	v_pk_mul_f32 v[12:13], v[12:13], v[126:127]
	v_pk_mul_f32 v[8:9], v[8:9], v[158:159]
	s_waitcnt lgkmcnt(0)
	v_pk_mul_f32 v[4:5], v[4:5], v[162:163]
	v_pk_mul_f32 v[2:3], v[2:3], v[160:161]
	v_pk_mul_f32 v[30:31], v[30:31], v[120:121]
	v_pk_mul_f32 v[26:27], v[26:27], v[124:125]
	v_pk_mul_f32 v[22:23], v[22:23], v[156:157]
	v_pk_mul_f32 v[32:33], v[32:33], v[122:123]
	v_pk_mul_f32 v[28:29], v[28:29], v[126:127]
	v_pk_mul_f32 v[24:25], v[24:25], v[158:159]
	v_pk_mul_f32 v[20:21], v[20:21], v[162:163]
	v_pk_mul_f32 v[18:19], v[18:19], v[160:161]
.LBB0_586:
	v_cndmask_b32_e64 v155, v114, v118, s[6:7]
	v_mul_f32_e32 v156, 0xbfb8aa3b, v155
	v_fmamk_f32 v50, v50, 0x3fb8aa3b, v156
	v_fmamk_f32 v51, v51, 0x3fb8aa3b, v156
	v_fmamk_f32 v52, v52, 0x3fb8aa3b, v156
	v_fmamk_f32 v53, v53, 0x3fb8aa3b, v156
	v_fmamk_f32 v54, v54, 0x3fb8aa3b, v156
	v_fmamk_f32 v55, v55, 0x3fb8aa3b, v156
	v_fmamk_f32 v56, v56, 0x3fb8aa3b, v156
	v_fmamk_f32 v57, v57, 0x3fb8aa3b, v156
	v_fmamk_f32 v58, v58, 0x3fb8aa3b, v156
	v_fmamk_f32 v59, v59, 0x3fb8aa3b, v156
	v_fmamk_f32 v60, v60, 0x3fb8aa3b, v156
	v_fmamk_f32 v61, v61, 0x3fb8aa3b, v156
	v_fmamk_f32 v62, v62, 0x3fb8aa3b, v156
	v_fmamk_f32 v63, v63, 0x3fb8aa3b, v156
	v_fmamk_f32 v64, v64, 0x3fb8aa3b, v156
	v_fmamk_f32 v65, v65, 0x3fb8aa3b, v156
	v_exp_f32_e32 v114, v50
	v_exp_f32_e32 v129, v51
	v_exp_f32_e32 v115, v52
	v_exp_f32_e32 v128, v53
	v_exp_f32_e32 v116, v54
	v_exp_f32_e32 v127, v55
	v_exp_f32_e32 v117, v56
	v_exp_f32_e32 v126, v57
	v_exp_f32_e32 v118, v58
	v_exp_f32_e32 v125, v59
	v_exp_f32_e32 v119, v60
	v_exp_f32_e32 v124, v61
	v_exp_f32_e32 v120, v62
	v_exp_f32_e32 v123, v63
	v_exp_f32_e32 v121, v64
	v_exp_f32_e32 v122, v65
	v_fmamk_f32 v161, v44, 0x3fb8aa3b, v156
	v_fmamk_f32 v162, v45, 0x3fb8aa3b, v156
	v_fmamk_f32 v164, v34, 0x3fb8aa3b, v156
	v_fmamk_f32 v165, v35, 0x3fb8aa3b, v156
	v_fmamk_f32 v171, v36, 0x3fb8aa3b, v156
	v_fmamk_f32 v172, v37, 0x3fb8aa3b, v156
	v_fmamk_f32 v173, v38, 0x3fb8aa3b, v156
	v_fmamk_f32 v174, v39, 0x3fb8aa3b, v156
	v_fmamk_f32 v157, v40, 0x3fb8aa3b, v156
	v_fmamk_f32 v158, v41, 0x3fb8aa3b, v156
	v_fmamk_f32 v159, v42, 0x3fb8aa3b, v156
	v_fmamk_f32 v160, v43, 0x3fb8aa3b, v156
	v_fmamk_f32 v163, v46, 0x3fb8aa3b, v156
	v_fmamk_f32 v175, v47, 0x3fb8aa3b, v156
	v_fmamk_f32 v176, v48, 0x3fb8aa3b, v156
	v_fmac_f32_e32 v156, 0x3fb8aa3b, v49
	s_waitcnt lgkmcnt(0)
	s_barrier
	ds_read_b128 v[34:37], v145 offset:16384
	ds_read_b128 v[38:41], v145 offset:24576
	ds_read_b128 v[178:181], v148 offset:16384
	ds_read_b128 v[182:185], v148 offset:24576
	v_exp_f32_e32 v166, v171
	v_exp_f32_e32 v171, v173
	s_waitcnt lgkmcnt(3)
	v_mfma_f32_32x32x16_bf16 v[50:65], v[34:37], v[86:89], 0
	v_exp_f32_e32 v173, v161
	v_add_f32_e32 v161, 0, v114
	v_add_f32_e32 v161, v129, v161
	v_add_f32_e32 v161, v115, v161
	v_add_f32_e32 v161, v128, v161
	v_add_f32_e32 v161, v116, v161
	v_add_f32_e32 v161, v127, v161
	s_waitcnt lgkmcnt(2)
	v_mfma_f32_32x32x16_bf16 v[34:49], v[38:41], v[86:89], 0
	v_add_f32_e32 v161, v117, v161
	v_add_f32_e32 v161, v126, v161
	v_add_f32_e32 v161, v118, v161
	v_add_f32_e32 v161, v125, v161
	v_add_f32_e32 v161, v119, v161
	v_add_f32_e32 v161, v124, v161
	v_exp_f32_e32 v164, v164
	s_waitcnt lgkmcnt(1)
	v_mfma_f32_32x32x16_bf16 v[50:65], v[178:181], v[74:77], v[50:65]
	v_add_f32_e32 v161, v120, v161
	v_exp_f32_e32 v165, v165
	v_add_f32_e32 v161, v123, v161
	v_add_f32_e32 v161, v121, v161
	v_exp_f32_e32 v167, v172
	v_add_f32_e32 v161, v122, v161
	v_add_f32_e32 v161, v164, v161
	s_waitcnt lgkmcnt(0)
	v_mfma_f32_32x32x16_bf16 v[34:49], v[182:185], v[74:77], v[34:49]
	ds_read_b128 v[178:181], v147 offset:16384
	ds_read_b128 v[182:185], v147 offset:24576
	v_exp_f32_e32 v172, v174
	v_add_f32_e32 v161, v165, v161
	v_exp_f32_e32 v157, v157
	v_add_f32_e32 v161, v166, v161
	v_exp_f32_e32 v158, v158
	v_add_f32_e32 v161, v167, v161
	s_waitcnt lgkmcnt(1)
	v_mfma_f32_32x32x16_bf16 v[50:65], v[178:181], v[70:73], v[50:65]
	v_exp_f32_e32 v159, v159
	v_add_f32_e32 v161, v171, v161
	v_exp_f32_e32 v160, v160
	v_add_f32_e32 v161, v172, v161
	v_add_f32_e32 v161, v157, v161
	v_exp_f32_e32 v174, v162
	v_add_f32_e32 v161, v158, v161
	s_waitcnt lgkmcnt(0)
	v_mfma_f32_32x32x16_bf16 v[34:49], v[182:185], v[70:73], v[34:49]
	ds_read_b128 v[178:181], v146 offset:16384
	ds_read_b128 v[182:185], v146 offset:24576
	v_exp_f32_e32 v163, v163
	v_add_f32_e32 v161, v159, v161
	v_exp_f32_e32 v175, v175
	v_add_f32_e32 v161, v160, v161
	v_exp_f32_e32 v176, v176
	v_add_f32_e32 v161, v173, v161
	s_waitcnt lgkmcnt(1)
	v_mfma_f32_32x32x16_bf16 v[50:65], v[178:181], v[82:85], v[50:65]
	v_exp_f32_e32 v156, v156
	v_add_f32_e32 v161, v174, v161
	v_add_f32_e32 v161, v163, v161
	v_add_f32_e32 v161, v175, v161
	v_add_f32_e32 v161, v176, v161
	v_add_f32_e32 v161, v156, v161
	v_mov_b32_e32 v162, v161
	s_waitcnt lgkmcnt(0)
	v_mfma_f32_32x32x16_bf16 v[34:49], v[182:185], v[82:85], v[34:49]
	ds_read_b128 v[178:181], v150 offset:16384
	ds_read_b128 v[182:185], v150 offset:24576
	v_permlane32_swap_b32_e32 v161, v162
	s_waitcnt lgkmcnt(1)
	v_mfma_f32_32x32x16_bf16 v[50:65], v[178:181], v[78:81], v[50:65]
	s_waitcnt lgkmcnt(0)
	v_mfma_f32_32x32x16_bf16 v[34:49], v[182:185], v[78:81], v[34:49]
	ds_read_b128 v[178:181], v149 offset:16384
	ds_read_b128 v[182:185], v149 offset:24576
	v_cvt_pk_bf16_f32 v114, v114, v129
	v_cvt_pk_bf16_f32 v115, v115, v128
	v_cvt_pk_bf16_f32 v116, v116, v127
	v_cvt_pk_bf16_f32 v117, v117, v126
	v_cvt_pk_bf16_f32 v118, v118, v125
	v_cvt_pk_bf16_f32 v119, v119, v124
	s_waitcnt lgkmcnt(1)
	v_mfma_f32_32x32x16_bf16 v[50:65], v[178:181], v[66:69], v[50:65]
	v_cvt_pk_bf16_f32 v120, v120, v123
	v_cvt_pk_bf16_f32 v121, v121, v122
	v_cvt_pk_bf16_f32 v122, v164, v165
	v_cvt_pk_bf16_f32 v123, v166, v167
	v_cvt_pk_bf16_f32 v124, v171, v172
	v_cvt_pk_bf16_f32 v125, v157, v158
	v_cvt_pk_bf16_f32 v126, v159, v160
	s_waitcnt lgkmcnt(0)
	v_mfma_f32_32x32x16_bf16 v[34:49], v[182:185], v[66:69], v[34:49]
	ds_read_b64_tr_b16 v[186:187], v139 offset:0
	ds_read_b64_tr_b16 v[188:189], v139 offset:0x400
	ds_read_b64_tr_b16 v[190:191], v139 offset:0x800
	ds_read_b64_tr_b16 v[192:193], v139 offset:0xc00
	ds_read_b64_tr_b16 v[194:195], v139 offset:0x1000
	ds_read_b64_tr_b16 v[196:197], v139 offset:0x1400
	ds_read_b64_tr_b16 v[198:199], v139 offset:0x1800
	ds_read_b64_tr_b16 v[200:201], v139 offset:0x1c00
	v_cvt_pk_bf16_f32 v127, v173, v174
	v_cvt_pk_bf16_f32 v128, v163, v175
	v_cvt_pk_bf16_f32 v129, v176, v156
	v_permlane32_swap_b32_e32 v114, v116
	v_permlane32_swap_b32_e32 v115, v117
	v_permlane32_swap_b32_e32 v118, v120
	v_permlane32_swap_b32_e32 v119, v121
	v_permlane32_swap_b32_e32 v122, v124
	v_permlane32_swap_b32_e32 v123, v125
	v_permlane32_swap_b32_e32 v126, v128
	v_permlane32_swap_b32_e32 v127, v129
	s_cmp_ge_u32 s35, s34
	s_cselect_b64 s[0:1], -1, 0
	s_and_b64 vcc, exec, s[0:1]
	s_cbranch_vccnz .LBB0_588
	v_add_co_u32_e32 v94, vcc, 0xffffe000, v132
	global_load_dwordx4 v[90:93], v[134:135], off
	s_nop 0
	v_addc_co_u32_e32 v95, vcc, -1, v133, vcc
	global_load_dwordx4 v[98:101], v[94:95], off
	s_nop 0
	global_load_dwordx4 v[94:97], v[132:133], off
.LBB0_588:
	ds_read_b64_tr_b16 v[156:157], v139 offset:0x200
	ds_read_b64_tr_b16 v[158:159], v139 offset:0x600
	ds_read_b64_tr_b16 v[172:173], v139 offset:0xa00
	ds_read_b64_tr_b16 v[174:175], v139 offset:0xe00
	ds_read_b64_tr_b16 v[176:177], v139 offset:0x1200
	ds_read_b64_tr_b16 v[178:179], v139 offset:0x1600
	ds_read_b64_tr_b16 v[180:181], v139 offset:0x1a00
	ds_read_b64_tr_b16 v[182:183], v139 offset:0x1e00
	s_waitcnt lgkmcnt(8)
	s_nop 0
	v_mfma_f32_32x32x16_bf16 v[2:17], v[114:117], v[186:189], v[2:17]
	v_mfma_f32_32x32x16_bf16 v[2:17], v[118:121], v[190:193], v[2:17]
	v_mfma_f32_32x32x16_bf16 v[2:17], v[122:125], v[194:197], v[2:17]
	v_mfma_f32_32x32x16_bf16 v[2:17], v[126:129], v[198:201], v[2:17]
	s_waitcnt lgkmcnt(0)
	v_mfma_f32_32x32x16_bf16 v[18:33], v[114:117], v[156:159], v[18:33]
	v_max_f32_e32 v114, v51, v51
	v_max_f32_e32 v115, v50, v50
	v_max_f32_e32 v114, v115, v114
	v_max3_f32 v114, v114, v52, v53
	v_max3_f32 v114, v114, v54, v55
	v_max3_f32 v114, v114, v56, v57
	v_max3_f32 v114, v114, v58, v59
	v_max3_f32 v114, v114, v60, v61
	v_max3_f32 v114, v114, v62, v63
	v_mfma_f32_32x32x16_bf16 v[18:33], v[118:121], v[172:175], v[18:33]
	v_max3_f32 v114, v114, v64, v65
	v_max3_f32 v114, v114, v34, v35
	v_max3_f32 v114, v114, v36, v37
	v_max3_f32 v114, v114, v38, v39
	v_max3_f32 v114, v114, v40, v41
	v_max3_f32 v114, v114, v42, v43
	v_max3_f32 v114, v114, v44, v45
	v_max3_f32 v114, v114, v46, v47
	v_mfma_f32_32x32x16_bf16 v[18:33], v[122:125], v[176:179], v[18:33]
	v_max3_f32 v114, v114, v48, v49
	v_mov_b32_e32 v115, v114
	s_nop 1
	v_permlane32_swap_b32_e32 v114, v115
	v_max_f32_e32 v115, v115, v115
	v_max_f32_e32 v114, v114, v114
	v_max_f32_e32 v114, v114, v115
	v_sub_f32_e32 v115, v114, v155
	v_cmp_ge_f32_e32 vcc, s93, v115
	v_max_f32_e32 v115, v155, v155
	v_max_f32_e32 v114, v115, v114
	v_mfma_f32_32x32x16_bf16 v[18:33], v[126:129], v[180:183], v[18:33]
	v_sub_f32_e32 v115, v155, v114
	v_mul_f32_e32 v115, 0x3fb8aa3b, v115
	v_exp_f32_e32 v115, v115
	s_cmp_eq_u64 vcc, exec
	s_cselect_b64 s[6:7], -1, 0
	s_barrier
	s_waitcnt vmcnt(3)
	v_cndmask_b32_e64 v119, v115, 1.0, s[6:7]
	v_cmp_gt_f32_e32 vcc, 1.0, v119
	s_waitcnt vmcnt(2)
	ds_write_b128 v144, v[102:105] offset:8192
	s_waitcnt vmcnt(1)
	ds_write_b128 v142, v[106:109] offset:32768
	s_waitcnt vmcnt(0)
	ds_write_b128 v143, v[110:113] offset:32768
	s_cbranch_vccz .LBB0_592
	s_and_saveexec_b64 s[24:25], s[4:5]
	ds_write_b32 v138, v119 offset:49280
	s_or_b64 exec, exec, s[24:25]
	s_waitcnt lgkmcnt(0)
	v_add_u32_e32 v115, v131, v226
	ds_read_b128 v[102:105], v115 offset:49376
	ds_read_b128 v[106:109], v115 offset:49344
	ds_read_b128 v[110:113], v115 offset:49312
	ds_read_b128 v[120:123], v115 offset:49280
	s_waitcnt lgkmcnt(3)
	v_pk_mul_f32 v[14:15], v[14:15], v[102:103]
	s_waitcnt lgkmcnt(2)
	v_pk_mul_f32 v[10:11], v[10:11], v[106:107]
	s_waitcnt lgkmcnt(1)
	v_pk_mul_f32 v[6:7], v[6:7], v[110:111]
	v_pk_mul_f32 v[16:17], v[16:17], v[104:105]
	v_pk_mul_f32 v[12:13], v[12:13], v[108:109]
	v_pk_mul_f32 v[8:9], v[8:9], v[112:113]
	s_waitcnt lgkmcnt(0)
	v_pk_mul_f32 v[4:5], v[4:5], v[122:123]
	v_pk_mul_f32 v[2:3], v[2:3], v[120:121]
	v_pk_mul_f32 v[30:31], v[30:31], v[102:103]
	v_pk_mul_f32 v[26:27], v[26:27], v[106:107]
	v_pk_mul_f32 v[22:23], v[22:23], v[110:111]
	v_pk_mul_f32 v[32:33], v[32:33], v[104:105]
	v_pk_mul_f32 v[28:29], v[28:29], v[108:109]
	v_pk_mul_f32 v[24:25], v[24:25], v[112:113]
	v_pk_mul_f32 v[20:21], v[20:21], v[122:123]
	v_pk_mul_f32 v[18:19], v[18:19], v[120:121]
